# P@V loop: transposed reads of k-step ks issued before the MFMAs of k-step ks-1 (double-buffered fragments), V loads emitted in saddr form by the generator (on top of v59)
# speedup vs baseline: 1.0033x; 1.0033x over previous
.LBB0_1334:
	v_and_b32_e32 v34, 64, v209
	v_max_f32_e32 v21, v215, v215
	v_mov_b32_e32 v32, v141
	v_mov_b32_e32 v33, v141
	v_max_f32_e32 v20, v215, v215
	v_readlane_b32 s9, v254, 54
	s_movk_i32 s8, 0x520
	v_lshlrev_b32_e32 v34, 2, v34
	v_permlane16_swap_b32_e32 v20, v21
	s_lshl_b64 s[0:1], s[0:1], 9
	s_lshl_b64 s[0:1], s[0:1], 1
	v_max_f32_e32 v20, v20, v21
	v_mov_b32_e32 v21, v20
	s_nop 1
	v_permlane32_swap_b32_e32 v20, v21
	s_nop 1
	v_max_f32_e32 v20, v20, v21
	v_add_f32_e32 v20, 0xc1000000, v20
	v_pk_add_f32 v[118:119], v[118:119], v[20:21] op_sel_hi:[1,0] neg_lo:[0,1] neg_hi:[0,1]
	v_pk_add_f32 v[120:121], v[120:121], v[20:21] op_sel_hi:[1,0] neg_lo:[0,1] neg_hi:[0,1]
	v_pk_add_f32 v[122:123], v[122:123], v[20:21] op_sel_hi:[1,0] neg_lo:[0,1] neg_hi:[0,1]
	v_pk_add_f32 v[124:125], v[124:125], v[20:21] op_sel_hi:[1,0] neg_lo:[0,1] neg_hi:[0,1]
	v_pk_add_f32 v[126:127], v[126:127], v[20:21] op_sel_hi:[1,0] neg_lo:[0,1] neg_hi:[0,1]
	v_pk_add_f32 v[128:129], v[128:129], v[20:21] op_sel_hi:[1,0] neg_lo:[0,1] neg_hi:[0,1]
	v_pk_add_f32 v[130:131], v[130:131], v[20:21] op_sel_hi:[1,0] neg_lo:[0,1] neg_hi:[0,1]
	v_pk_add_f32 v[132:133], v[132:133], v[20:21] op_sel_hi:[1,0] neg_lo:[0,1] neg_hi:[0,1]
	v_pk_add_f32 v[134:135], v[134:135], v[20:21] op_sel_hi:[1,0] neg_lo:[0,1] neg_hi:[0,1]
	v_pk_add_f32 v[136:137], v[136:137], v[20:21] op_sel_hi:[1,0] neg_lo:[0,1] neg_hi:[0,1]
	v_pk_add_f32 v[156:157], v[156:157], v[20:21] op_sel_hi:[1,0] neg_lo:[0,1] neg_hi:[0,1]
	v_pk_add_f32 v[158:159], v[158:159], v[20:21] op_sel_hi:[1,0] neg_lo:[0,1] neg_hi:[0,1]
	v_pk_add_f32 v[160:161], v[160:161], v[20:21] op_sel_hi:[1,0] neg_lo:[0,1] neg_hi:[0,1]
	v_pk_add_f32 v[162:163], v[162:163], v[20:21] op_sel_hi:[1,0] neg_lo:[0,1] neg_hi:[0,1]
	v_pk_add_f32 v[164:165], v[164:165], v[20:21] op_sel_hi:[1,0] neg_lo:[0,1] neg_hi:[0,1]
	v_pk_add_f32 v[166:167], v[166:167], v[20:21] op_sel_hi:[1,0] neg_lo:[0,1] neg_hi:[0,1]
	v_pk_add_f32 v[168:169], v[168:169], v[20:21] op_sel_hi:[1,0] neg_lo:[0,1] neg_hi:[0,1]
	v_pk_add_f32 v[170:171], v[170:171], v[20:21] op_sel_hi:[1,0] neg_lo:[0,1] neg_hi:[0,1]
	v_pk_add_f32 v[172:173], v[172:173], v[20:21] op_sel_hi:[1,0] neg_lo:[0,1] neg_hi:[0,1]
	v_pk_add_f32 v[174:175], v[174:175], v[20:21] op_sel_hi:[1,0] neg_lo:[0,1] neg_hi:[0,1]
	v_pk_add_f32 v[176:177], v[176:177], v[20:21] op_sel_hi:[1,0] neg_lo:[0,1] neg_hi:[0,1]
	v_pk_add_f32 v[178:179], v[178:179], v[20:21] op_sel_hi:[1,0] neg_lo:[0,1] neg_hi:[0,1]
	v_pk_add_f32 v[180:181], v[180:181], v[20:21] op_sel_hi:[1,0] neg_lo:[0,1] neg_hi:[0,1]
	v_pk_add_f32 v[182:183], v[182:183], v[20:21] op_sel_hi:[1,0] neg_lo:[0,1] neg_hi:[0,1]
	v_pk_add_f32 v[184:185], v[184:185], v[20:21] op_sel_hi:[1,0] neg_lo:[0,1] neg_hi:[0,1]
	v_pk_add_f32 v[186:187], v[186:187], v[20:21] op_sel_hi:[1,0] neg_lo:[0,1] neg_hi:[0,1]
	v_pk_add_f32 v[188:189], v[188:189], v[20:21] op_sel_hi:[1,0] neg_lo:[0,1] neg_hi:[0,1]
	v_pk_add_f32 v[190:191], v[190:191], v[20:21] op_sel_hi:[1,0] neg_lo:[0,1] neg_hi:[0,1]
	v_pk_add_f32 v[192:193], v[192:193], v[20:21] op_sel_hi:[1,0] neg_lo:[0,1] neg_hi:[0,1]
	v_pk_add_f32 v[194:195], v[194:195], v[20:21] op_sel_hi:[1,0] neg_lo:[0,1] neg_hi:[0,1]
	v_pk_add_f32 v[196:197], v[196:197], v[20:21] op_sel_hi:[1,0] neg_lo:[0,1] neg_hi:[0,1]
	v_pk_add_f32 v[198:199], v[198:199], v[20:21] op_sel_hi:[1,0] neg_lo:[0,1] neg_hi:[0,1]
	v_exp_f32_e32 v21, v118
	v_exp_f32_e32 v23, v119
	v_exp_f32_e32 v24, v120
	v_exp_f32_e32 v25, v121
	v_exp_f32_e32 v26, v122
	v_exp_f32_e32 v27, v123
	v_exp_f32_e32 v28, v124
	v_exp_f32_e32 v29, v125
	v_exp_f32_e32 v31, v126
	v_exp_f32_e32 v36, v127
	v_exp_f32_e32 v37, v128
	v_exp_f32_e32 v38, v129
	v_exp_f32_e32 v39, v130
	v_exp_f32_e32 v40, v131
	v_exp_f32_e32 v41, v132
	v_exp_f32_e32 v42, v133
	v_exp_f32_e32 v43, v134
	v_exp_f32_e32 v44, v135
	v_exp_f32_e32 v45, v136
	v_exp_f32_e32 v46, v137
	v_exp_f32_e32 v47, v156
	v_exp_f32_e32 v48, v157
	v_exp_f32_e32 v49, v158
	v_exp_f32_e32 v50, v159
	v_exp_f32_e32 v51, v160
	v_exp_f32_e32 v52, v161
	v_exp_f32_e32 v53, v162
	v_exp_f32_e32 v54, v163
	v_exp_f32_e32 v55, v164
	v_exp_f32_e32 v56, v165
	v_exp_f32_e32 v57, v166
	v_exp_f32_e32 v58, v167
	v_exp_f32_e32 v59, v168
	v_exp_f32_e32 v60, v169
	v_exp_f32_e32 v61, v170
	v_exp_f32_e32 v62, v171
	v_exp_f32_e32 v63, v172
	v_exp_f32_e32 v64, v173
	v_exp_f32_e32 v65, v174
	v_exp_f32_e32 v66, v175
	v_exp_f32_e32 v67, v176
	v_exp_f32_e32 v68, v177
	v_exp_f32_e32 v69, v178
	v_exp_f32_e32 v70, v179
	v_exp_f32_e32 v71, v180
	v_exp_f32_e32 v72, v181
	v_exp_f32_e32 v73, v182
	v_exp_f32_e32 v74, v183
	v_exp_f32_e32 v75, v184
	v_exp_f32_e32 v76, v185
	v_exp_f32_e32 v77, v186
	v_exp_f32_e32 v78, v187
	v_exp_f32_e32 v79, v188
	v_exp_f32_e32 v80, v189
	v_exp_f32_e32 v81, v190
	v_exp_f32_e32 v82, v191
	v_exp_f32_e32 v83, v192
	v_exp_f32_e32 v84, v193
	v_exp_f32_e32 v85, v194
	v_exp_f32_e32 v86, v195
	v_exp_f32_e32 v87, v196
	v_exp_f32_e32 v88, v197
	v_exp_f32_e32 v89, v198
	v_exp_f32_e32 v90, v199
	s_nop 0
	v_pk_add_f32 v[118:119], v[24:25], v[38:39]
	v_pk_add_f32 v[120:121], v[26:27], v[40:41]
	v_pk_add_f32 v[122:123], v[28:29], v[42:43]
	v_pk_add_f32 v[124:125], v[36:37], v[44:45]
	v_pk_add_f32 v[118:119], v[118:119], v[46:47]
	v_pk_add_f32 v[120:121], v[120:121], v[48:49]
	v_pk_add_f32 v[122:123], v[122:123], v[50:51]
	v_pk_add_f32 v[124:125], v[124:125], v[52:53]
	v_pk_add_f32 v[118:119], v[118:119], v[54:55]
	v_pk_add_f32 v[120:121], v[120:121], v[56:57]
	v_pk_add_f32 v[122:123], v[122:123], v[58:59]
	v_pk_add_f32 v[124:125], v[124:125], v[60:61]
	v_pk_add_f32 v[118:119], v[118:119], v[62:63]
	v_pk_add_f32 v[120:121], v[120:121], v[64:65]
	v_pk_add_f32 v[122:123], v[122:123], v[66:67]
	v_pk_add_f32 v[124:125], v[124:125], v[68:69]
	v_pk_add_f32 v[118:119], v[118:119], v[70:71]
	v_pk_add_f32 v[120:121], v[120:121], v[72:73]
	v_pk_add_f32 v[122:123], v[122:123], v[74:75]
	v_pk_add_f32 v[124:125], v[124:125], v[76:77]
	v_pk_add_f32 v[118:119], v[118:119], v[78:79]
	v_pk_add_f32 v[120:121], v[120:121], v[80:81]
	v_pk_add_f32 v[122:123], v[122:123], v[82:83]
	v_pk_add_f32 v[124:125], v[124:125], v[84:85]
	v_pk_add_f32 v[118:119], v[118:119], v[86:87]
	v_pk_add_f32 v[120:121], v[120:121], v[88:89]
	v_pk_add_f32 v[118:119], v[118:119], v[120:121]
	v_pk_add_f32 v[122:123], v[122:123], v[124:125]
	v_add_f32_e32 v126, v21, v23
	v_add_f32_e32 v127, v31, v90
	v_pk_add_f32 v[118:119], v[118:119], v[122:123]
	v_add_f32_e32 v126, v126, v127
	v_add_f32_e32 v20, v118, v119
	v_add_f32_e32 v20, v20, v126
	v_mov_b32_e32 v18, v20
	v_cvt_pk_fp8_f32 v32, v21, v23
	v_cvt_pk_fp8_f32 v33, v26, v27
	v_permlane16_swap_b32_e32 v18, v20
	v_mov_b32_e32 v30, v141
	v_cvt_pk_fp8_f32 v30, v31, v36
	v_add_f32_e32 v18, v20, v18
	v_mov_b32_e32 v19, v18
	v_cvt_pk_fp8_f32 v32, v24, v25 op_sel:[0,0,1]
	v_cvt_pk_fp8_f32 v33, v28, v29 op_sel:[0,0,1]
	v_permlane32_swap_b32_e32 v18, v19
	v_mov_b32_e32 v31, v141
	v_mov_b32_e32 v28, v141
	v_add_f32_e32 v35, v18, v19
	v_mov_b32_e32 v29, v141
	v_mov_b32_e32 v24, v141
	v_mov_b32_e32 v25, v141
	v_mov_b32_e32 v22, v141
	v_mov_b32_e32 v23, v141
	v_mov_b32_e32 v20, v141
	v_mov_b32_e32 v21, v141
	v_mov_b32_e32 v18, v141
	v_mov_b32_e32 v19, v141
	v_mov_b32_e32 v26, v141
	v_mov_b32_e32 v27, v141
	v_cvt_pk_fp8_f32 v31, v39, v40
	v_cvt_pk_fp8_f32 v28, v43, v44
	v_cvt_pk_fp8_f32 v29, v47, v48
	v_cvt_pk_fp8_f32 v24, v51, v52
	v_cvt_pk_fp8_f32 v25, v55, v56
	v_cvt_pk_fp8_f32 v22, v59, v60
	v_cvt_pk_fp8_f32 v23, v63, v64
	v_cvt_pk_fp8_f32 v20, v67, v68
	v_cvt_pk_fp8_f32 v21, v71, v72
	v_cvt_pk_fp8_f32 v18, v75, v76
	v_cvt_pk_fp8_f32 v19, v79, v80
	v_cvt_pk_fp8_f32 v26, v83, v84
	v_cvt_pk_fp8_f32 v27, v87, v88
	v_cvt_pk_fp8_f32 v30, v37, v38 op_sel:[0,0,1]
	v_cvt_pk_fp8_f32 v31, v41, v42 op_sel:[0,0,1]
	v_cvt_pk_fp8_f32 v28, v45, v46 op_sel:[0,0,1]
	v_cvt_pk_fp8_f32 v29, v49, v50 op_sel:[0,0,1]
	v_cvt_pk_fp8_f32 v24, v53, v54 op_sel:[0,0,1]
	v_cvt_pk_fp8_f32 v25, v57, v58 op_sel:[0,0,1]
	v_cvt_pk_fp8_f32 v22, v61, v62 op_sel:[0,0,1]
	v_cvt_pk_fp8_f32 v23, v65, v66 op_sel:[0,0,1]
	v_cvt_pk_fp8_f32 v20, v69, v70 op_sel:[0,0,1]
	v_cvt_pk_fp8_f32 v21, v73, v74 op_sel:[0,0,1]
	v_cvt_pk_fp8_f32 v18, v77, v78 op_sel:[0,0,1]
	v_cvt_pk_fp8_f32 v19, v81, v82 op_sel:[0,0,1]
	v_cvt_pk_fp8_f32 v26, v85, v86 op_sel:[0,0,1]
	v_cvt_pk_fp8_f32 v27, v89, v90 op_sel:[0,0,1]
	s_nop 0
	ds_read_u16 v86, v212 offset:64
	ds_read_u16 v87, v212 offset:80
	ds_read_u16 v88, v212 offset:96
	ds_read_u16 v89, v212 offset:112
	ds_read_u16 v90, v212 offset:128
	ds_read_u16 v91, v212 offset:144
	ds_read_u16 v92, v212 offset:160
	ds_read_u16 v93, v212 offset:176
	ds_read_u16 v94, v212 offset:192
	ds_read_u16 v95, v212 offset:208
	ds_read_u16 v96, v212 offset:224
	ds_read_u16 v97, v212 offset:240
	ds_read_u16 v98, v212 offset:256
	ds_read_u16 v99, v212 offset:272
	ds_read_u16 v100, v212 offset:288
	ds_read_u16 v101, v212 offset:304
	ds_read_u16 v102, v212 offset:320
	ds_read_u16 v103, v212 offset:336
	ds_read_u16 v104, v212 offset:352
	ds_read_u16 v105, v212 offset:368
	ds_read_u16 v106, v212 offset:384
	ds_read_u16 v107, v212 offset:400
	ds_read_u16 v108, v212 offset:416
	ds_read_u16 v109, v212 offset:432
	ds_read_u16 v110, v212 offset:448
	ds_read_u16 v111, v212 offset:464
	ds_read_u16 v112, v212 offset:480
	ds_read_u16 v113, v212 offset:496
	v_ashrrev_i32_e32 v36, 1, v210
	v_cmp_gt_i32_e32 vcc, 4, v36
	v_add_u32_e32 v37, 12, v117
	v_mov_b32_e32 v54, s9
	v_cndmask_b32_e32 v37, v37, v117, vcc
	v_add_u32_e32 v36, v37, v36
	v_and_b32_e32 v37, 15, v36
	v_mad_u32_u24 v37, v37, s24, v54
	v_lshrrev_b32_e32 v36, 4, v36
	v_lshlrev_b32_e32 v54, 3, v210
	v_mul_lo_u32 v36, v36, s8
	v_and_b32_e32 v54, 8, v54
	v_add3_u32 v36, v37, v36, v54
	v_lshrrev_b32_e32 v37, 2, v214
	s_movk_i32 s8, 0xa40
	v_mul_lo_u32 v37, v37, s8
	v_add_u32_e32 v37, s9, v37
	v_and_b32_e32 v54, 48, v116
	v_mul_lo_u32 v55, v213, s24
	v_add3_u32 v37, v37, v54, v55
	s_waitcnt lgkmcnt(0)
	v_lshl_add_u32 v244, v86, 7, v116
	global_load_dwordx4 v[38:41], v244, s[48:49]
	v_lshl_add_u32 v246, v87, 7, v116
	global_load_dwordx4 v[42:45], v246, s[48:49]
	v_lshl_add_u32 v248, v88, 7, v116
	global_load_dwordx4 v[46:49], v248, s[48:49]
	v_lshl_add_u32 v250, v89, 7, v116
	global_load_dwordx4 v[50:53], v250, s[48:49]
	v_lshl_add_u32 v244, v90, 7, v116
	global_load_dwordx4 v[156:159], v244, s[48:49]
	v_lshl_add_u32 v246, v91, 7, v116
	global_load_dwordx4 v[160:163], v246, s[48:49]
	v_lshl_add_u32 v248, v92, 7, v116
	global_load_dwordx4 v[164:167], v248, s[48:49]
	v_lshl_add_u32 v250, v93, 7, v116
	global_load_dwordx4 v[168:171], v250, s[48:49]
	v_lshl_add_u32 v244, v94, 7, v116
	global_load_dwordx4 v[172:175], v244, s[48:49]
	v_lshl_add_u32 v246, v95, 7, v116
	global_load_dwordx4 v[176:179], v246, s[48:49]
	v_lshl_add_u32 v248, v96, 7, v116
	global_load_dwordx4 v[180:183], v248, s[48:49]
	v_lshl_add_u32 v250, v97, 7, v116
	global_load_dwordx4 v[184:187], v250, s[48:49]
	v_lshl_add_u32 v244, v98, 7, v116
	global_load_dwordx4 v[188:191], v244, s[48:49]
	v_lshl_add_u32 v246, v99, 7, v116
	global_load_dwordx4 v[192:195], v246, s[48:49]
	v_lshl_add_u32 v248, v100, 7, v116
	global_load_dwordx4 v[196:199], v248, s[48:49]
	v_lshl_add_u32 v250, v101, 7, v116
	global_load_dwordx4 v[224:227], v250, s[48:49]
	v_lshl_add_u32 v244, v102, 7, v116
	global_load_dwordx4 v[228:231], v244, s[48:49]
	v_lshl_add_u32 v246, v103, 7, v116
	global_load_dwordx4 v[232:235], v246, s[48:49]
	v_lshl_add_u32 v248, v104, 7, v116
	global_load_dwordx4 v[236:239], v248, s[48:49]
	v_lshl_add_u32 v250, v105, 7, v116
	global_load_dwordx4 v[240:243], v250, s[48:49]
	s_waitcnt vmcnt(23)
	ds_write_b128 v37, v[2:5]
	s_waitcnt vmcnt(22)
	ds_write_b128 v37, v[6:9] offset:640
	s_waitcnt vmcnt(21)
	ds_write_b128 v37, v[10:13] offset:1312
	s_waitcnt vmcnt(20)
	ds_write_b128 v37, v[14:17] offset:1952
	v_lshl_add_u32 v244, v106, 7, v116
	global_load_dwordx4 v[2:5], v244, s[48:49]
	v_lshl_add_u32 v246, v107, 7, v116
	global_load_dwordx4 v[6:9], v246, s[48:49]
	v_lshl_add_u32 v248, v108, 7, v116
	global_load_dwordx4 v[10:13], v248, s[48:49]
	v_lshl_add_u32 v250, v109, 7, v116
	global_load_dwordx4 v[14:17], v250, s[48:49]
	s_waitcnt lgkmcnt(0)
	ds_read_b64_tr_b8 v[86:87], v36 offset:0
	ds_read_b64_tr_b8 v[88:89], v36 offset:16
	ds_read_b64_tr_b8 v[90:91], v36 offset:32
	ds_read_b64_tr_b8 v[92:93], v36 offset:48
	ds_read_b64_tr_b8 v[94:95], v36 offset:2624
	ds_read_b64_tr_b8 v[96:97], v36 offset:2640
	ds_read_b64_tr_b8 v[98:99], v36 offset:2656
	ds_read_b64_tr_b8 v[100:101], v36 offset:2672
	s_waitcnt lgkmcnt(0)
	s_waitcnt vmcnt(23)
	ds_write_b128 v37, v[38:41]
	s_waitcnt vmcnt(22)
	ds_write_b128 v37, v[42:45] offset:640
	s_waitcnt vmcnt(21)
	ds_write_b128 v37, v[46:49] offset:1312
	s_waitcnt vmcnt(20)
	ds_write_b128 v37, v[50:53] offset:1952
	v_lshl_add_u32 v244, v110, 7, v116
	global_load_dwordx4 v[38:41], v244, s[48:49]
	v_lshl_add_u32 v246, v111, 7, v116
	global_load_dwordx4 v[42:45], v246, s[48:49]
	v_lshl_add_u32 v248, v112, 7, v116
	global_load_dwordx4 v[46:49], v248, s[48:49]
	v_lshl_add_u32 v250, v113, 7, v116
	global_load_dwordx4 v[50:53], v250, s[48:49]
	s_waitcnt lgkmcnt(0)
	ds_read_b64_tr_b8 v[118:119], v36 offset:0
	ds_read_b64_tr_b8 v[120:121], v36 offset:16
	ds_read_b64_tr_b8 v[122:123], v36 offset:32
	ds_read_b64_tr_b8 v[124:125], v36 offset:48
	ds_read_b64_tr_b8 v[126:127], v36 offset:2624
	ds_read_b64_tr_b8 v[128:129], v36 offset:2640
	ds_read_b64_tr_b8 v[130:131], v36 offset:2656
	ds_read_b64_tr_b8 v[132:133], v36 offset:2672
	v_mfma_f32_16x16x32_fp8_fp8 v[54:57], v[32:33], v[86:87], 0
	v_mfma_f32_16x16x32_fp8_fp8 v[58:61], v[32:33], v[88:89], 0
	v_mfma_f32_16x16x32_fp8_fp8 v[62:65], v[32:33], v[90:91], 0
	v_mfma_f32_16x16x32_fp8_fp8 v[66:69], v[32:33], v[92:93], 0
	v_mfma_f32_16x16x32_fp8_fp8 v[70:73], v[32:33], v[94:95], 0
	v_mfma_f32_16x16x32_fp8_fp8 v[74:77], v[32:33], v[96:97], 0
	v_mfma_f32_16x16x32_fp8_fp8 v[78:81], v[32:33], v[98:99], 0
	v_mfma_f32_16x16x32_fp8_fp8 v[82:85], v[32:33], v[100:101], 0
	s_waitcnt lgkmcnt(0)
	s_waitcnt vmcnt(23)
	ds_write_b128 v37, v[156:159]
	s_waitcnt vmcnt(22)
	ds_write_b128 v37, v[160:163] offset:640
	s_waitcnt vmcnt(21)
	ds_write_b128 v37, v[164:167] offset:1312
	s_waitcnt vmcnt(20)
	ds_write_b128 v37, v[168:171] offset:1952
	s_waitcnt lgkmcnt(0)
	ds_read_b64_tr_b8 v[86:87], v36 offset:0
	ds_read_b64_tr_b8 v[88:89], v36 offset:16
	ds_read_b64_tr_b8 v[90:91], v36 offset:32
	ds_read_b64_tr_b8 v[92:93], v36 offset:48
	ds_read_b64_tr_b8 v[94:95], v36 offset:2624
	ds_read_b64_tr_b8 v[96:97], v36 offset:2640
	ds_read_b64_tr_b8 v[98:99], v36 offset:2656
	ds_read_b64_tr_b8 v[100:101], v36 offset:2672
	v_mfma_f32_16x16x32_fp8_fp8 v[54:57], v[30:31], v[118:119], v[54:57]
	v_mfma_f32_16x16x32_fp8_fp8 v[58:61], v[30:31], v[120:121], v[58:61]
	v_mfma_f32_16x16x32_fp8_fp8 v[62:65], v[30:31], v[122:123], v[62:65]
	v_mfma_f32_16x16x32_fp8_fp8 v[66:69], v[30:31], v[124:125], v[66:69]
	v_mfma_f32_16x16x32_fp8_fp8 v[70:73], v[30:31], v[126:127], v[70:73]
	v_mfma_f32_16x16x32_fp8_fp8 v[74:77], v[30:31], v[128:129], v[74:77]
	v_mfma_f32_16x16x32_fp8_fp8 v[78:81], v[30:31], v[130:131], v[78:81]
	v_mfma_f32_16x16x32_fp8_fp8 v[82:85], v[30:31], v[132:133], v[82:85]
	s_waitcnt lgkmcnt(0)
	s_waitcnt vmcnt(19)
	ds_write_b128 v37, v[172:175]
	s_waitcnt vmcnt(18)
	ds_write_b128 v37, v[176:179] offset:640
	s_waitcnt vmcnt(17)
	ds_write_b128 v37, v[180:183] offset:1312
	s_waitcnt vmcnt(16)
	ds_write_b128 v37, v[184:187] offset:1952
	s_waitcnt lgkmcnt(0)
	ds_read_b64_tr_b8 v[118:119], v36 offset:0
	ds_read_b64_tr_b8 v[120:121], v36 offset:16
	ds_read_b64_tr_b8 v[122:123], v36 offset:32
	ds_read_b64_tr_b8 v[124:125], v36 offset:48
	ds_read_b64_tr_b8 v[126:127], v36 offset:2624
	ds_read_b64_tr_b8 v[128:129], v36 offset:2640
	ds_read_b64_tr_b8 v[130:131], v36 offset:2656
	ds_read_b64_tr_b8 v[132:133], v36 offset:2672
	v_mfma_f32_16x16x32_fp8_fp8 v[54:57], v[28:29], v[86:87], v[54:57]
	v_mfma_f32_16x16x32_fp8_fp8 v[58:61], v[28:29], v[88:89], v[58:61]
	v_mfma_f32_16x16x32_fp8_fp8 v[62:65], v[28:29], v[90:91], v[62:65]
	v_mfma_f32_16x16x32_fp8_fp8 v[66:69], v[28:29], v[92:93], v[66:69]
	v_mfma_f32_16x16x32_fp8_fp8 v[70:73], v[28:29], v[94:95], v[70:73]
	v_mfma_f32_16x16x32_fp8_fp8 v[74:77], v[28:29], v[96:97], v[74:77]
	v_mfma_f32_16x16x32_fp8_fp8 v[78:81], v[28:29], v[98:99], v[78:81]
	v_mfma_f32_16x16x32_fp8_fp8 v[82:85], v[28:29], v[100:101], v[82:85]
	s_waitcnt lgkmcnt(0)
	s_waitcnt vmcnt(15)
	ds_write_b128 v37, v[188:191]
	s_waitcnt vmcnt(14)
	ds_write_b128 v37, v[192:195] offset:640
	s_waitcnt vmcnt(13)
	ds_write_b128 v37, v[196:199] offset:1312
	s_waitcnt vmcnt(12)
	ds_write_b128 v37, v[224:227] offset:1952
	s_waitcnt lgkmcnt(0)
	ds_read_b64_tr_b8 v[86:87], v36 offset:0
	ds_read_b64_tr_b8 v[88:89], v36 offset:16
	ds_read_b64_tr_b8 v[90:91], v36 offset:32
	ds_read_b64_tr_b8 v[92:93], v36 offset:48
	ds_read_b64_tr_b8 v[94:95], v36 offset:2624
	ds_read_b64_tr_b8 v[96:97], v36 offset:2640
	ds_read_b64_tr_b8 v[98:99], v36 offset:2656
	ds_read_b64_tr_b8 v[100:101], v36 offset:2672
	v_mfma_f32_16x16x32_fp8_fp8 v[54:57], v[24:25], v[118:119], v[54:57]
	v_mfma_f32_16x16x32_fp8_fp8 v[58:61], v[24:25], v[120:121], v[58:61]
	v_mfma_f32_16x16x32_fp8_fp8 v[62:65], v[24:25], v[122:123], v[62:65]
	v_mfma_f32_16x16x32_fp8_fp8 v[66:69], v[24:25], v[124:125], v[66:69]
	v_mfma_f32_16x16x32_fp8_fp8 v[70:73], v[24:25], v[126:127], v[70:73]
	v_mfma_f32_16x16x32_fp8_fp8 v[74:77], v[24:25], v[128:129], v[74:77]
	v_mfma_f32_16x16x32_fp8_fp8 v[78:81], v[24:25], v[130:131], v[78:81]
	v_mfma_f32_16x16x32_fp8_fp8 v[82:85], v[24:25], v[132:133], v[82:85]
	s_waitcnt lgkmcnt(0)
	s_waitcnt vmcnt(11)
	ds_write_b128 v37, v[228:231]
	s_waitcnt vmcnt(10)
	ds_write_b128 v37, v[232:235] offset:640
	s_waitcnt vmcnt(9)
	ds_write_b128 v37, v[236:239] offset:1312
	s_waitcnt vmcnt(8)
	ds_write_b128 v37, v[240:243] offset:1952
	s_waitcnt lgkmcnt(0)
	ds_read_b64_tr_b8 v[118:119], v36 offset:0
	ds_read_b64_tr_b8 v[120:121], v36 offset:16
	ds_read_b64_tr_b8 v[122:123], v36 offset:32
	ds_read_b64_tr_b8 v[124:125], v36 offset:48
	ds_read_b64_tr_b8 v[126:127], v36 offset:2624
	ds_read_b64_tr_b8 v[128:129], v36 offset:2640
	ds_read_b64_tr_b8 v[130:131], v36 offset:2656
	ds_read_b64_tr_b8 v[132:133], v36 offset:2672
	v_mfma_f32_16x16x32_fp8_fp8 v[54:57], v[22:23], v[86:87], v[54:57]
	v_mfma_f32_16x16x32_fp8_fp8 v[58:61], v[22:23], v[88:89], v[58:61]
	v_mfma_f32_16x16x32_fp8_fp8 v[62:65], v[22:23], v[90:91], v[62:65]
	v_mfma_f32_16x16x32_fp8_fp8 v[66:69], v[22:23], v[92:93], v[66:69]
	v_mfma_f32_16x16x32_fp8_fp8 v[70:73], v[22:23], v[94:95], v[70:73]
	v_mfma_f32_16x16x32_fp8_fp8 v[74:77], v[22:23], v[96:97], v[74:77]
	v_mfma_f32_16x16x32_fp8_fp8 v[78:81], v[22:23], v[98:99], v[78:81]
	v_mfma_f32_16x16x32_fp8_fp8 v[82:85], v[22:23], v[100:101], v[82:85]
	s_waitcnt lgkmcnt(0)
	s_waitcnt vmcnt(7)
	ds_write_b128 v37, v[2:5]
	s_waitcnt vmcnt(6)
	ds_write_b128 v37, v[6:9] offset:640
	s_waitcnt vmcnt(5)
	ds_write_b128 v37, v[10:13] offset:1312
	s_waitcnt vmcnt(4)
	ds_write_b128 v37, v[14:17] offset:1952
	s_waitcnt lgkmcnt(0)
	ds_read_b64_tr_b8 v[86:87], v36 offset:0
	ds_read_b64_tr_b8 v[88:89], v36 offset:16
	ds_read_b64_tr_b8 v[90:91], v36 offset:32
	ds_read_b64_tr_b8 v[92:93], v36 offset:48
	ds_read_b64_tr_b8 v[94:95], v36 offset:2624
	ds_read_b64_tr_b8 v[96:97], v36 offset:2640
	ds_read_b64_tr_b8 v[98:99], v36 offset:2656
	ds_read_b64_tr_b8 v[100:101], v36 offset:2672
	v_mfma_f32_16x16x32_fp8_fp8 v[54:57], v[20:21], v[118:119], v[54:57]
	v_mfma_f32_16x16x32_fp8_fp8 v[58:61], v[20:21], v[120:121], v[58:61]
	v_mfma_f32_16x16x32_fp8_fp8 v[62:65], v[20:21], v[122:123], v[62:65]
	v_mfma_f32_16x16x32_fp8_fp8 v[66:69], v[20:21], v[124:125], v[66:69]
	v_mfma_f32_16x16x32_fp8_fp8 v[70:73], v[20:21], v[126:127], v[70:73]
	v_mfma_f32_16x16x32_fp8_fp8 v[74:77], v[20:21], v[128:129], v[74:77]
	v_mfma_f32_16x16x32_fp8_fp8 v[78:81], v[20:21], v[130:131], v[78:81]
	v_mfma_f32_16x16x32_fp8_fp8 v[82:85], v[20:21], v[132:133], v[82:85]
	s_waitcnt lgkmcnt(0)
	s_waitcnt vmcnt(3)
	ds_write_b128 v37, v[38:41]
	s_waitcnt vmcnt(2)
	ds_write_b128 v37, v[42:45] offset:640
	s_waitcnt vmcnt(1)
	ds_write_b128 v37, v[46:49] offset:1312
	s_waitcnt vmcnt(0)
	ds_write_b128 v37, v[50:53] offset:1952
	s_waitcnt lgkmcnt(0)
	ds_read_b64_tr_b8 v[118:119], v36 offset:0
	ds_read_b64_tr_b8 v[120:121], v36 offset:16
	ds_read_b64_tr_b8 v[122:123], v36 offset:32
	ds_read_b64_tr_b8 v[124:125], v36 offset:48
	ds_read_b64_tr_b8 v[126:127], v36 offset:2624
	ds_read_b64_tr_b8 v[128:129], v36 offset:2640
	ds_read_b64_tr_b8 v[130:131], v36 offset:2656
	ds_read_b64_tr_b8 v[132:133], v36 offset:2672
	v_mfma_f32_16x16x32_fp8_fp8 v[54:57], v[18:19], v[86:87], v[54:57]
	v_mfma_f32_16x16x32_fp8_fp8 v[58:61], v[18:19], v[88:89], v[58:61]
	v_mfma_f32_16x16x32_fp8_fp8 v[62:65], v[18:19], v[90:91], v[62:65]
	v_mfma_f32_16x16x32_fp8_fp8 v[66:69], v[18:19], v[92:93], v[66:69]
	v_mfma_f32_16x16x32_fp8_fp8 v[70:73], v[18:19], v[94:95], v[70:73]
	v_mfma_f32_16x16x32_fp8_fp8 v[74:77], v[18:19], v[96:97], v[74:77]
	v_mfma_f32_16x16x32_fp8_fp8 v[78:81], v[18:19], v[98:99], v[78:81]
	v_mfma_f32_16x16x32_fp8_fp8 v[82:85], v[18:19], v[100:101], v[82:85]
	s_waitcnt lgkmcnt(0)
	v_mfma_f32_16x16x32_fp8_fp8 v[2:5], v[26:27], v[118:119], v[54:57]
	v_mfma_f32_16x16x32_fp8_fp8 v[6:9], v[26:27], v[120:121], v[58:61]
	v_mfma_f32_16x16x32_fp8_fp8 v[10:13], v[26:27], v[122:123], v[62:65]
	v_mfma_f32_16x16x32_fp8_fp8 v[14:17], v[26:27], v[124:125], v[66:69]
	v_mfma_f32_16x16x32_fp8_fp8 v[18:21], v[26:27], v[126:127], v[70:73]
	v_mfma_f32_16x16x32_fp8_fp8 v[22:25], v[26:27], v[128:129], v[74:77]
	v_mfma_f32_16x16x32_fp8_fp8 v[30:33], v[26:27], v[130:131], v[78:81]
	v_mfma_f32_16x16x32_fp8_fp8 v[26:29], v[26:27], v[132:133], v[82:85]
	v_div_scale_f32 v36, s[8:9], v35, v35, 1.0
	v_rcp_f32_e32 v37, v36
	v_readlane_b32 s8, v254, 62
	s_add_u32 s0, s8, s0
	v_readlane_b32 s8, v254, 63
	s_addc_u32 s1, s8, s1
	v_cmp_gt_i32_e64 s[8:9], 2, v211
	v_fma_f32 v38, -v36, v37, 1.0
	v_fmac_f32_e32 v37, v38, v37
	v_div_scale_f32 v38, vcc, 1.0, v35, 1.0
	v_mul_f32_e32 v39, v38, v37
	v_fma_f32 v40, -v36, v39, v38
	v_fmac_f32_e32 v39, v40, v37
	v_fma_f32 v36, -v36, v39, v38
	v_div_fmas_f32 v36, v36, v37, v39
	v_div_fixup_f32 v35, v36, v35, 1.0
	ds_bpermute_b32 v36, v34, v35
	ds_bpermute_b32 v37, v34, v35 offset:16
	v_cmp_eq_u32_e32 vcc, 0, v211
	s_and_saveexec_b64 s[10:11], s[8:9]
	s_cbranch_execz .LBB0_1336
	v_lshl_add_u32 v38, v211, 8, v210
	v_cndmask_b32_e32 v2, v18, v2, vcc
	s_waitcnt lgkmcnt(0)
	v_cndmask_b32_e32 v18, v37, v36, vcc
	v_mul_f32_e32 v2, v2, v18
	v_ashrrev_i32_e32 v39, 31, v38
	v_cvt_pk_bf16_f32 v2, v2, s0
	v_lshl_add_u64 v[36:37], v[38:39], 1, s[0:1]
	global_store_short v[36:37], v2, off
	v_cndmask_b32_e32 v2, v22, v6, vcc
	v_mul_f32_e32 v2, v2, v18
	v_cvt_pk_bf16_f32 v2, v2, s0
	global_store_short v[36:37], v2, off offset:32
	v_cndmask_b32_e32 v2, v30, v10, vcc
	v_mul_f32_e32 v2, v2, v18
	v_cvt_pk_bf16_f32 v2, v2, s0
	global_store_short v[36:37], v2, off offset:64
	v_cndmask_b32_e32 v2, v26, v14, vcc
	v_mul_f32_e32 v2, v2, v18
	v_cvt_pk_bf16_f32 v2, v2, s0
	global_store_short v[36:37], v2, off offset:96
